# v52 + differential-attention unit epilogue: parked pass-1 tile re-read and gain loads batched (1+2 round trips instead of ~32 serialized load/wait/store steps)
# baseline (speedup 1.0000x reference)
.LBB6_1287:
	v_and_b32_e32 v2, 63, v145
	v_lshlrev_b32_e32 v2, 2, v2
	s_barrier
	global_load_dword v68, v2, s[10:11]
	global_load_dword v69, v2, s[14:15]
	global_load_dwordx2 v[230:231], v[128:129], off
	global_load_dwordx2 v[232:233], v[128:129], off offset:16
	global_load_dwordx2 v[234:235], v[128:129], off offset:32
	global_load_dwordx2 v[236:237], v[128:129], off offset:48
	global_load_dwordx2 v[238:239], v[128:129], off offset:64
	global_load_dwordx2 v[240:241], v[128:129], off offset:80
	global_load_dwordx2 v[242:243], v[128:129], off offset:96
	global_load_dwordx2 v[244:245], v[128:129], off offset:112
	global_load_dwordx2 v[246:247], v[128:129], off offset:128
	global_load_dwordx2 v[248:249], v[128:129], off offset:144
	global_load_dwordx2 v[250:251], v[128:129], off offset:160
	global_load_dwordx2 v[252:253], v[128:129], off offset:176
	global_load_dwordx2 v[216:217], v[128:129], off offset:192
	global_load_dwordx2 v[218:219], v[128:129], off offset:208
	global_load_dwordx2 v[220:221], v[128:129], off offset:224
	global_load_dwordx2 v[222:223], v[128:129], off offset:240
	v_xor_b32_e32 v71, 1, v213
	v_cmp_lt_i32_e32 vcc, v71, v146
	v_mov_b32_e32 v89, v54
	v_mov_b32_e32 v54, v53
	v_cndmask_b32_e32 v71, v213, v71, vcc
	v_lshlrev_b32_e32 v71, 2, v71
	v_mov_b32_e32 v88, v52
	v_mov_b32_e32 v91, v58
	v_mov_b32_e32 v58, v57
	v_mov_b32_e32 v90, v56
	v_mov_b32_e32 v93, v62
	v_mov_b32_e32 v62, v61
	v_mov_b32_e32 v92, v60
	v_mov_b32_e32 v95, v66
	v_mov_b32_e32 v66, v65
	v_mov_b32_e32 v94, v64
	v_mov_b32_e32 v97, v38
	v_mov_b32_e32 v38, v37
	v_mov_b32_e32 v96, v36
	v_mov_b32_e32 v99, v42
	v_mov_b32_e32 v42, v41
	v_mov_b32_e32 v98, v40
	v_mov_b32_e32 v101, v46
	v_mov_b32_e32 v46, v45
	v_mov_b32_e32 v100, v44
	v_mov_b32_e32 v103, v50
	v_mov_b32_e32 v50, v49
	v_mov_b32_e32 v102, v48
	v_mov_b32_e32 v105, v22
	v_mov_b32_e32 v22, v21
	v_mov_b32_e32 v104, v20
	v_mov_b32_e32 v107, v26
	v_mov_b32_e32 v26, v25
	v_mov_b32_e32 v106, v24
	v_mov_b32_e32 v109, v30
	v_mov_b32_e32 v30, v29
	v_mov_b32_e32 v108, v28
	v_mov_b32_e32 v111, v34
	v_mov_b32_e32 v34, v33
	v_mov_b32_e32 v110, v32
	s_waitcnt vmcnt(0)
	v_mul_f32_e32 v70, v68, v69
	ds_bpermute_b32 v70, v71, v70
	s_waitcnt lgkmcnt(0)
	v_fmac_f32_e32 v70, v68, v69
	v_xor_b32_e32 v68, 2, v213
	v_cmp_lt_i32_e32 vcc, v68, v146
	s_nop 1
	v_cndmask_b32_e32 v68, v213, v68, vcc
	v_lshlrev_b32_e32 v68, 2, v68
	ds_bpermute_b32 v69, v68, v70
	s_waitcnt lgkmcnt(0)
	v_add_f32_e32 v69, v70, v69
	v_xor_b32_e32 v70, 4, v213
	v_cmp_lt_i32_e32 vcc, v70, v146
	s_nop 1
	v_cndmask_b32_e32 v70, v213, v70, vcc
	v_lshlrev_b32_e32 v70, 2, v70
	ds_bpermute_b32 v72, v70, v69
	s_waitcnt lgkmcnt(0)
	v_add_f32_e32 v69, v69, v72
	v_xor_b32_e32 v72, 8, v213
	v_cmp_lt_i32_e32 vcc, v72, v146
	s_nop 1
	v_cndmask_b32_e32 v72, v213, v72, vcc
	v_lshlrev_b32_e32 v72, 2, v72
	ds_bpermute_b32 v73, v72, v69
	s_waitcnt lgkmcnt(0)
	v_add_f32_e32 v69, v69, v73
	v_xor_b32_e32 v73, 16, v213
	v_cmp_lt_i32_e32 vcc, v73, v146
	s_nop 1
	v_cndmask_b32_e32 v73, v213, v73, vcc
	v_lshlrev_b32_e32 v73, 2, v73
	ds_bpermute_b32 v74, v73, v69
	s_waitcnt lgkmcnt(0)
	v_add_f32_e32 v69, v69, v74
	ds_bpermute_b32 v74, v131, v69
	s_waitcnt lgkmcnt(0)
	v_add_f32_e32 v69, v69, v74
	global_load_dword v74, v2, s[16:17]
	s_nop 0
	global_load_dword v2, v2, s[18:19]
	v_mul_f32_e32 v69, 0x3fb8aa3b, v69
	v_exp_f32_e32 v69, v69
	s_waitcnt vmcnt(0)
	v_mul_f32_e32 v75, v74, v2
	ds_bpermute_b32 v71, v71, v75
	s_waitcnt lgkmcnt(0)
	v_fmac_f32_e32 v71, v74, v2
	ds_bpermute_b32 v2, v68, v71
	s_waitcnt lgkmcnt(0)
	v_add_f32_e32 v2, v71, v2
	ds_bpermute_b32 v68, v70, v2
	s_waitcnt lgkmcnt(0)
	v_add_f32_e32 v2, v2, v68
	ds_bpermute_b32 v68, v72, v2
	s_waitcnt lgkmcnt(0)
	v_add_f32_e32 v2, v2, v68
	ds_bpermute_b32 v68, v73, v2
	s_waitcnt lgkmcnt(0)
	v_add_f32_e32 v2, v2, v68
	ds_bpermute_b32 v68, v131, v2
	s_waitcnt lgkmcnt(0)
	v_add_f32_e32 v2, v2, v68
	v_mul_f32_e32 v2, 0x3fb8aa3b, v2
	v_exp_f32_e32 v2, v2
	s_nop 0
	v_sub_f32_e32 v68, v69, v2
	ds_bpermute_b32 v69, v131, v183
	s_waitcnt lgkmcnt(0)
	v_pk_add_f32 v[68:69], v[182:183], v[68:69]
	s_nop 0
	v_div_scale_f32 v2, s[0:1], v69, v69, v68
	v_rcp_f32_e32 v70, v2
	s_nop 0
	v_fma_f32 v71, -v2, v70, 1.0
	v_fmac_f32_e32 v70, v71, v70
	v_div_scale_f32 v71, vcc, v68, v69, v68
	v_mul_f32_e32 v72, v71, v70
	v_fma_f32 v73, -v2, v72, v71
	v_fmac_f32_e32 v72, v73, v70
	v_fma_f32 v2, -v2, v72, v71
	v_div_fmas_f32 v2, v2, v70, v72
	v_div_fixup_f32 v2, v2, v69, v68
	v_mov_b64_e32 v[68:69], v[230:231]
	v_mov_b64_e32 v[70:71], v[238:239]
	v_lshlrev_b32_e32 v72, 16, v68
	v_and_b32_e32 v73, 0xffff0000, v68
	v_lshlrev_b32_e32 v76, 16, v69
	v_and_b32_e32 v77, 0xffff0000, v69
	v_mov_b64_e32 v[68:69], v[232:233]
	v_pk_fma_f32 v[6:7], v[6:7], v[2:3], v[76:77] op_sel_hi:[1,0,1] neg_lo:[1,0,0] neg_hi:[1,0,0]
	v_pk_fma_f32 v[4:5], v[4:5], v[2:3], v[72:73] op_sel_hi:[1,0,1] neg_lo:[1,0,0] neg_hi:[1,0,0]
	v_mul_f32_e32 v76, v7, v7
	v_mul_f32_e32 v72, v5, v5
	v_pk_fma_f32 v[76:77], v[6:7], v[6:7], v[76:77] op_sel_hi:[1,1,0]
	v_pk_fma_f32 v[72:73], v[4:5], v[4:5], v[72:73] op_sel_hi:[1,1,0]
	v_lshlrev_b32_e32 v74, 16, v68
	v_and_b32_e32 v75, 0xffff0000, v68
	v_lshlrev_b32_e32 v78, 16, v69
	v_and_b32_e32 v79, 0xffff0000, v69
	v_mov_b64_e32 v[68:69], v[234:235]
	v_pk_fma_f32 v[10:11], v[10:11], v[2:3], v[78:79] op_sel_hi:[1,0,1] neg_lo:[1,0,0] neg_hi:[1,0,0]
	v_pk_fma_f32 v[8:9], v[8:9], v[2:3], v[74:75] op_sel_hi:[1,0,1] neg_lo:[1,0,0] neg_hi:[1,0,0]
	v_pk_add_f32 v[72:73], v[72:73], v[76:77]
	v_mul_f32_e32 v76, v11, v11
	v_mul_f32_e32 v74, v9, v9
	v_pk_fma_f32 v[76:77], v[10:11], v[10:11], v[76:77] op_sel_hi:[1,1,0]
	v_pk_fma_f32 v[74:75], v[8:9], v[8:9], v[74:75] op_sel_hi:[1,1,0]
	v_lshlrev_b32_e32 v80, 16, v68
	v_and_b32_e32 v81, 0xffff0000, v68
	v_lshlrev_b32_e32 v84, 16, v69
	v_and_b32_e32 v85, 0xffff0000, v69
	v_mov_b64_e32 v[68:69], v[236:237]
	v_pk_add_f32 v[74:75], v[74:75], v[76:77]
	v_pk_fma_f32 v[14:15], v[14:15], v[2:3], v[84:85] op_sel_hi:[1,0,1] neg_lo:[1,0,0] neg_hi:[1,0,0]
	v_pk_fma_f32 v[12:13], v[12:13], v[2:3], v[80:81] op_sel_hi:[1,0,1] neg_lo:[1,0,0] neg_hi:[1,0,0]
	v_pk_add_f32 v[72:73], v[72:73], v[74:75]
	v_mul_f32_e32 v74, v15, v15
	v_mul_f32_e32 v76, v13, v13
	v_pk_fma_f32 v[74:75], v[14:15], v[14:15], v[74:75] op_sel_hi:[1,1,0]
	v_pk_fma_f32 v[76:77], v[12:13], v[12:13], v[76:77] op_sel_hi:[1,1,0]
	v_lshlrev_b32_e32 v82, 16, v68
	v_and_b32_e32 v83, 0xffff0000, v68
	v_lshlrev_b32_e32 v86, 16, v69
	v_and_b32_e32 v87, 0xffff0000, v69
	v_lshlrev_b32_e32 v69, 16, v71
	v_lshlrev_b32_e32 v68, 16, v70
	v_and_b32_e32 v71, 0xffff0000, v71
	v_and_b32_e32 v70, 0xffff0000, v70
	v_pk_fma_f32 v[52:53], v[54:55], v[2:3], v[70:71] op_sel_hi:[1,0,1] neg_lo:[1,0,0] neg_hi:[1,0,0]
	v_pk_fma_f32 v[68:69], v[88:89], v[2:3], v[68:69] op_sel_hi:[1,0,1] neg_lo:[1,0,0] neg_hi:[1,0,0]
	v_pk_mul_f32 v[54:55], v[52:53], v[52:53]
	v_pk_add_f32 v[74:75], v[76:77], v[74:75]
	v_pk_fma_f32 v[54:55], v[68:69], v[68:69], v[54:55]
	v_pk_fma_f32 v[18:19], v[18:19], v[2:3], v[86:87] op_sel_hi:[1,0,1] neg_lo:[1,0,0] neg_hi:[1,0,0]
	v_pk_add_f32 v[88:89], v[54:55], v[54:55] op_sel:[0,1] op_sel_hi:[1,0]
	v_mov_b64_e32 v[54:55], v[240:241]
	v_pk_fma_f32 v[16:17], v[16:17], v[2:3], v[82:83] op_sel_hi:[1,0,1] neg_lo:[1,0,0] neg_hi:[1,0,0]
	v_pk_add_f32 v[72:73], v[72:73], v[74:75]
	v_mul_f32_e32 v74, v19, v19
	v_pk_fma_f32 v[74:75], v[18:19], v[18:19], v[74:75] op_sel_hi:[1,1,0]
	v_lshlrev_b32_e32 v71, 16, v55
	v_lshlrev_b32_e32 v70, 16, v54
	v_and_b32_e32 v55, 0xffff0000, v55
	v_and_b32_e32 v54, 0xffff0000, v54
	v_pk_fma_f32 v[54:55], v[58:59], v[2:3], v[54:55] op_sel_hi:[1,0,1] neg_lo:[1,0,0] neg_hi:[1,0,0]
	v_mov_b64_e32 v[58:59], v[242:243]
	v_pk_fma_f32 v[70:71], v[90:91], v[2:3], v[70:71] op_sel_hi:[1,0,1] neg_lo:[1,0,0] neg_hi:[1,0,0]
	v_pk_mul_f32 v[56:57], v[54:55], v[54:55]
	s_nop 0
	v_pk_fma_f32 v[56:57], v[70:71], v[70:71], v[56:57]
	s_nop 0
	v_pk_add_f32 v[90:91], v[56:57], v[56:57] op_sel:[0,1] op_sel_hi:[1,0]
	v_lshlrev_b32_e32 v57, 16, v59
	v_lshlrev_b32_e32 v56, 16, v58
	v_and_b32_e32 v59, 0xffff0000, v59
	v_and_b32_e32 v58, 0xffff0000, v58
	v_pk_fma_f32 v[62:63], v[62:63], v[2:3], v[58:59] op_sel_hi:[1,0,1] neg_lo:[1,0,0] neg_hi:[1,0,0]
	v_pk_fma_f32 v[56:57], v[92:93], v[2:3], v[56:57] op_sel_hi:[1,0,1] neg_lo:[1,0,0] neg_hi:[1,0,0]
	v_pk_mul_f32 v[58:59], v[62:63], v[62:63]
	s_nop 0
	v_pk_fma_f32 v[58:59], v[56:57], v[56:57], v[58:59]
	s_nop 0
	v_pk_add_f32 v[92:93], v[58:59], v[58:59] op_sel:[0,1] op_sel_hi:[1,0]
	v_mov_b64_e32 v[58:59], v[244:245]
	v_lshlrev_b32_e32 v61, 16, v59
	v_lshlrev_b32_e32 v60, 16, v58
	v_and_b32_e32 v59, 0xffff0000, v59
	v_and_b32_e32 v58, 0xffff0000, v58
	v_pk_fma_f32 v[58:59], v[66:67], v[2:3], v[58:59] op_sel_hi:[1,0,1] neg_lo:[1,0,0] neg_hi:[1,0,0]
	v_mov_b64_e32 v[66:67], v[246:247]
	v_pk_fma_f32 v[60:61], v[94:95], v[2:3], v[60:61] op_sel_hi:[1,0,1] neg_lo:[1,0,0] neg_hi:[1,0,0]
	v_pk_mul_f32 v[64:65], v[58:59], v[58:59]
	s_nop 0
	v_pk_fma_f32 v[64:65], v[60:61], v[60:61], v[64:65]
	s_nop 0
	v_pk_add_f32 v[94:95], v[64:65], v[64:65] op_sel:[0,1] op_sel_hi:[1,0]
	v_lshlrev_b32_e32 v65, 16, v67
	v_lshlrev_b32_e32 v64, 16, v66
	v_and_b32_e32 v67, 0xffff0000, v67
	v_and_b32_e32 v66, 0xffff0000, v66
	v_pk_fma_f32 v[36:37], v[38:39], v[2:3], v[66:67] op_sel_hi:[1,0,1] neg_lo:[1,0,0] neg_hi:[1,0,0]
	v_pk_fma_f32 v[64:65], v[96:97], v[2:3], v[64:65] op_sel_hi:[1,0,1] neg_lo:[1,0,0] neg_hi:[1,0,0]
	v_pk_mul_f32 v[38:39], v[36:37], v[36:37]
	s_nop 0
	v_pk_fma_f32 v[38:39], v[64:65], v[64:65], v[38:39]
	s_nop 0
	v_pk_add_f32 v[96:97], v[38:39], v[38:39] op_sel:[0,1] op_sel_hi:[1,0]
	v_mov_b64_e32 v[38:39], v[248:249]
	v_lshlrev_b32_e32 v67, 16, v39
	v_lshlrev_b32_e32 v66, 16, v38
	v_and_b32_e32 v39, 0xffff0000, v39
	v_and_b32_e32 v38, 0xffff0000, v38
	v_pk_fma_f32 v[38:39], v[42:43], v[2:3], v[38:39] op_sel_hi:[1,0,1] neg_lo:[1,0,0] neg_hi:[1,0,0]
	v_pk_fma_f32 v[66:67], v[98:99], v[2:3], v[66:67] op_sel_hi:[1,0,1] neg_lo:[1,0,0] neg_hi:[1,0,0]
	v_pk_mul_f32 v[40:41], v[38:39], v[38:39]
	s_nop 0
	v_pk_fma_f32 v[40:41], v[66:67], v[66:67], v[40:41]
	s_nop 0
	v_pk_add_f32 v[98:99], v[40:41], v[40:41] op_sel:[0,1] op_sel_hi:[1,0]
	v_mov_b64_e32 v[40:41], v[250:251]
	v_lshlrev_b32_e32 v43, 16, v41
	v_lshlrev_b32_e32 v42, 16, v40
	v_and_b32_e32 v41, 0xffff0000, v41
	v_and_b32_e32 v40, 0xffff0000, v40
	v_pk_fma_f32 v[40:41], v[46:47], v[2:3], v[40:41] op_sel_hi:[1,0,1] neg_lo:[1,0,0] neg_hi:[1,0,0]
	v_pk_fma_f32 v[42:43], v[100:101], v[2:3], v[42:43] op_sel_hi:[1,0,1] neg_lo:[1,0,0] neg_hi:[1,0,0]
	v_pk_mul_f32 v[44:45], v[40:41], v[40:41]
	s_nop 0
	v_pk_fma_f32 v[44:45], v[42:43], v[42:43], v[44:45]
	s_nop 0
	v_pk_add_f32 v[100:101], v[44:45], v[44:45] op_sel:[0,1] op_sel_hi:[1,0]
	v_mov_b64_e32 v[44:45], v[252:253]
	v_lshlrev_b32_e32 v47, 16, v45
	v_lshlrev_b32_e32 v46, 16, v44
	v_and_b32_e32 v45, 0xffff0000, v45
	v_and_b32_e32 v44, 0xffff0000, v44
	v_pk_fma_f32 v[44:45], v[50:51], v[2:3], v[44:45] op_sel_hi:[1,0,1] neg_lo:[1,0,0] neg_hi:[1,0,0]
	v_mov_b64_e32 v[50:51], v[216:217]
	v_pk_fma_f32 v[46:47], v[102:103], v[2:3], v[46:47] op_sel_hi:[1,0,1] neg_lo:[1,0,0] neg_hi:[1,0,0]
	v_pk_mul_f32 v[48:49], v[44:45], v[44:45]
	s_nop 0
	v_pk_fma_f32 v[48:49], v[46:47], v[46:47], v[48:49]
	s_nop 0
	v_pk_add_f32 v[102:103], v[48:49], v[48:49] op_sel:[0,1] op_sel_hi:[1,0]
	v_lshlrev_b32_e32 v49, 16, v51
	v_lshlrev_b32_e32 v48, 16, v50
	v_and_b32_e32 v51, 0xffff0000, v51
	v_and_b32_e32 v50, 0xffff0000, v50
	v_pk_fma_f32 v[20:21], v[22:23], v[2:3], v[50:51] op_sel_hi:[1,0,1] neg_lo:[1,0,0] neg_hi:[1,0,0]
	v_pk_fma_f32 v[48:49], v[104:105], v[2:3], v[48:49] op_sel_hi:[1,0,1] neg_lo:[1,0,0] neg_hi:[1,0,0]
	v_pk_mul_f32 v[22:23], v[20:21], v[20:21]
	s_nop 0
	v_pk_fma_f32 v[22:23], v[48:49], v[48:49], v[22:23]
	s_nop 0
	v_pk_add_f32 v[104:105], v[22:23], v[22:23] op_sel:[0,1] op_sel_hi:[1,0]
	v_mov_b64_e32 v[22:23], v[218:219]
	v_lshlrev_b32_e32 v51, 16, v23
	v_lshlrev_b32_e32 v50, 16, v22
	v_and_b32_e32 v23, 0xffff0000, v23
	v_and_b32_e32 v22, 0xffff0000, v22
	v_pk_fma_f32 v[22:23], v[26:27], v[2:3], v[22:23] op_sel_hi:[1,0,1] neg_lo:[1,0,0] neg_hi:[1,0,0]
	v_mov_b64_e32 v[26:27], v[220:221]
	v_pk_fma_f32 v[50:51], v[106:107], v[2:3], v[50:51] op_sel_hi:[1,0,1] neg_lo:[1,0,0] neg_hi:[1,0,0]
	v_pk_mul_f32 v[24:25], v[22:23], v[22:23]
	v_lshlrev_b32_e32 v107, 16, v27
	v_lshlrev_b32_e32 v106, 16, v26
	v_and_b32_e32 v27, 0xffff0000, v27
	v_and_b32_e32 v26, 0xffff0000, v26
	v_pk_fma_f32 v[26:27], v[30:31], v[2:3], v[26:27] op_sel_hi:[1,0,1] neg_lo:[1,0,0] neg_hi:[1,0,0]
	v_pk_fma_f32 v[106:107], v[108:109], v[2:3], v[106:107] op_sel_hi:[1,0,1] neg_lo:[1,0,0] neg_hi:[1,0,0]
	v_pk_mul_f32 v[28:29], v[26:27], v[26:27]
	v_pk_fma_f32 v[24:25], v[50:51], v[50:51], v[24:25]
	v_pk_fma_f32 v[28:29], v[106:107], v[106:107], v[28:29]
	v_pk_add_f32 v[24:25], v[24:25], v[24:25] op_sel:[0,1] op_sel_hi:[1,0]
	v_pk_add_f32 v[108:109], v[28:29], v[28:29] op_sel:[0,1] op_sel_hi:[1,0]
	v_mov_b64_e32 v[28:29], v[222:223]
	v_lshlrev_b32_e32 v31, 16, v29
	v_lshlrev_b32_e32 v30, 16, v28
	v_and_b32_e32 v29, 0xffff0000, v29
	v_and_b32_e32 v28, 0xffff0000, v28
	v_pk_fma_f32 v[28:29], v[34:35], v[2:3], v[28:29] op_sel_hi:[1,0,1] neg_lo:[1,0,0] neg_hi:[1,0,0]
	v_lshlrev_b32_e32 v34, 2, v130
	v_pk_fma_f32 v[30:31], v[110:111], v[2:3], v[30:31] op_sel_hi:[1,0,1] neg_lo:[1,0,0] neg_hi:[1,0,0]
	global_load_dwordx4 v[110:113], v34, s[20:21]
	global_load_dwordx4 v[230:233], v34, s[20:21] offset:32
	global_load_dwordx4 v[234:237], v34, s[20:21] offset:64
	global_load_dwordx4 v[238:241], v34, s[20:21] offset:96
	global_load_dwordx4 v[242:245], v34, s[20:21] offset:128
	global_load_dwordx4 v[246:249], v34, s[20:21] offset:160
	global_load_dwordx4 v[250:253], v34, s[20:21] offset:192
	global_load_dwordx4 v[216:219], v34, s[20:21] offset:224
	global_load_dwordx4 v[220:223], v34, s[20:21] offset:256
	v_mul_f32_e32 v2, v17, v17
	v_pk_fma_f32 v[76:77], v[16:17], v[16:17], v[2:3] op_sel_hi:[1,1,0]
	v_pk_mul_f32 v[32:33], v[28:29], v[28:29]
	v_pk_add_f32 v[74:75], v[76:77], v[74:75]
	v_pk_fma_f32 v[32:33], v[30:31], v[30:31], v[32:33]
	v_pk_add_f32 v[72:73], v[72:73], v[74:75]
	v_mov_b32_e32 v109, v33
	v_pk_add_f32 v[72:73], v[72:73], v[88:89]
	s_nop 0
	v_pk_add_f32 v[72:73], v[72:73], v[90:91]
	s_nop 0
	v_pk_add_f32 v[72:73], v[72:73], v[92:93]
	s_nop 0
	v_pk_add_f32 v[72:73], v[72:73], v[94:95]
	s_nop 0
	v_pk_add_f32 v[72:73], v[72:73], v[96:97]
	s_nop 0
	v_pk_add_f32 v[72:73], v[72:73], v[98:99]
	s_nop 0
	v_pk_add_f32 v[72:73], v[72:73], v[100:101]
	s_nop 0
	v_pk_add_f32 v[72:73], v[72:73], v[102:103]
	s_nop 0
	v_pk_add_f32 v[72:73], v[72:73], v[104:105]
	s_nop 0
	v_pk_add_f32 v[24:25], v[72:73], v[24:25]
	s_nop 0
	v_mov_b32_e32 v25, v32
	v_pk_add_f32 v[24:25], v[24:25], v[108:109]
	s_nop 0
	v_add_f32_e32 v2, v24, v25
	ds_bpermute_b32 v24, v131, v2
	s_waitcnt lgkmcnt(0)
	v_add_f32_e32 v2, v2, v24
	v_fmamk_f32 v2, v2, 0x3c000000, v212
	v_cmp_gt_f32_e32 vcc, s58, v2
	v_mul_f32_e32 v24, 0x4b800000, v2
	s_nop 0
	v_cndmask_b32_e32 v2, v2, v24, vcc
	v_rsq_f32_e32 v2, v2
	s_nop 0
	v_mul_f32_e32 v24, 0x45800000, v2
	v_cndmask_b32_e32 v2, v2, v24, vcc
	v_mul_f32_e32 v2, v228, v2
	v_pk_mul_f32 v[4:5], v[4:5], v[2:3] op_sel_hi:[1,0]
	v_pk_mul_f32 v[6:7], v[6:7], v[2:3] op_sel_hi:[1,0]
	v_pk_mul_f32 v[8:9], v[8:9], v[2:3] op_sel_hi:[1,0]
	s_waitcnt vmcnt(0)
	v_pk_mul_f32 v[4:5], v[110:111], v[4:5]
	v_pk_mul_f32 v[6:7], v[112:113], v[6:7]
	v_cvt_pk_bf16_f32 v4, v4, v5
	v_cvt_pk_bf16_f32 v5, v6, v7
	flat_store_dwordx2 v[128:129], v[4:5]
	v_mov_b64_e32 v[4:5], v[230:231]
	v_mov_b64_e32 v[6:7], v[232:233]
	v_pk_mul_f32 v[4:5], v[4:5], v[8:9]
	v_pk_mul_f32 v[8:9], v[10:11], v[2:3] op_sel_hi:[1,0]
	v_cvt_pk_bf16_f32 v4, v4, v5
	v_pk_mul_f32 v[6:7], v[6:7], v[8:9]
	v_pk_mul_f32 v[8:9], v[12:13], v[2:3] op_sel_hi:[1,0]
	v_cvt_pk_bf16_f32 v5, v6, v7
	flat_store_dwordx2 v[128:129], v[4:5] offset:16
	v_mov_b64_e32 v[4:5], v[234:235]
	v_mov_b64_e32 v[6:7], v[236:237]
	v_pk_mul_f32 v[4:5], v[4:5], v[8:9]
	v_pk_mul_f32 v[8:9], v[14:15], v[2:3] op_sel_hi:[1,0]
	v_cvt_pk_bf16_f32 v4, v4, v5
	v_pk_mul_f32 v[6:7], v[6:7], v[8:9]
	v_pk_mul_f32 v[8:9], v[16:17], v[2:3] op_sel_hi:[1,0]
	v_cvt_pk_bf16_f32 v5, v6, v7
	flat_store_dwordx2 v[128:129], v[4:5] offset:32
	v_mov_b64_e32 v[4:5], v[238:239]
	v_mov_b64_e32 v[6:7], v[240:241]
	v_pk_mul_f32 v[4:5], v[4:5], v[8:9]
	v_pk_mul_f32 v[8:9], v[18:19], v[2:3] op_sel_hi:[1,0]
	v_cvt_pk_bf16_f32 v4, v4, v5
	v_pk_mul_f32 v[6:7], v[6:7], v[8:9]
	v_mov_b32_e32 v8, v68
	v_cvt_pk_bf16_f32 v5, v6, v7
	flat_store_dwordx2 v[128:129], v[4:5] offset:48
	v_mov_b64_e32 v[4:5], v[242:243]
	v_mov_b64_e32 v[6:7], v[244:245]
	v_mov_b32_e32 v9, v52
	v_pk_mul_f32 v[8:9], v[8:9], v[2:3] op_sel_hi:[1,0]
	v_mov_b32_e32 v52, v69
	v_pk_mul_f32 v[4:5], v[4:5], v[8:9]
	v_pk_mul_f32 v[8:9], v[52:53], v[2:3] op_sel_hi:[1,0]
	v_cvt_pk_bf16_f32 v4, v4, v5
	v_pk_mul_f32 v[6:7], v[6:7], v[8:9]
	v_mov_b32_e32 v8, v70
	v_cvt_pk_bf16_f32 v5, v6, v7
	flat_store_dwordx2 v[128:129], v[4:5] offset:64
	v_mov_b64_e32 v[4:5], v[246:247]
	v_mov_b64_e32 v[6:7], v[248:249]
	v_mov_b32_e32 v9, v54
	v_pk_mul_f32 v[8:9], v[8:9], v[2:3] op_sel_hi:[1,0]
	v_mov_b32_e32 v54, v71
	v_pk_mul_f32 v[4:5], v[8:9], v[4:5]
	v_pk_mul_f32 v[8:9], v[54:55], v[2:3] op_sel_hi:[1,0]
	v_cvt_pk_bf16_f32 v4, v4, v5
	v_pk_mul_f32 v[6:7], v[8:9], v[6:7]
	v_mov_b32_e32 v8, v56
	v_cvt_pk_bf16_f32 v5, v6, v7
	flat_store_dwordx2 v[128:129], v[4:5] offset:80
	v_mov_b64_e32 v[4:5], v[250:251]
	v_mov_b64_e32 v[6:7], v[252:253]
	v_mov_b32_e32 v9, v62
	v_pk_mul_f32 v[8:9], v[8:9], v[2:3] op_sel_hi:[1,0]
	v_mov_b32_e32 v62, v57
	v_pk_mul_f32 v[4:5], v[8:9], v[4:5]
	v_pk_mul_f32 v[8:9], v[62:63], v[2:3] op_sel_hi:[1,0]
	v_cvt_pk_bf16_f32 v4, v4, v5
	v_pk_mul_f32 v[6:7], v[8:9], v[6:7]
	v_mov_b32_e32 v8, v60
	v_cvt_pk_bf16_f32 v5, v6, v7
	flat_store_dwordx2 v[128:129], v[4:5] offset:96
	v_mov_b64_e32 v[4:5], v[216:217]
	v_mov_b64_e32 v[6:7], v[218:219]
	v_mov_b32_e32 v9, v58
	v_pk_mul_f32 v[8:9], v[8:9], v[2:3] op_sel_hi:[1,0]
	v_mov_b32_e32 v58, v61
	v_pk_mul_f32 v[4:5], v[8:9], v[4:5]
	v_pk_mul_f32 v[8:9], v[58:59], v[2:3] op_sel_hi:[1,0]
	v_cvt_pk_bf16_f32 v4, v4, v5
	v_pk_mul_f32 v[6:7], v[8:9], v[6:7]
	v_mov_b32_e32 v8, v64
	v_cvt_pk_bf16_f32 v5, v6, v7
	flat_store_dwordx2 v[128:129], v[4:5] offset:112
	v_mov_b64_e32 v[4:5], v[220:221]
	v_mov_b64_e32 v[6:7], v[222:223]
	v_mov_b32_e32 v9, v36
	v_pk_mul_f32 v[8:9], v[8:9], v[2:3] op_sel_hi:[1,0]
	v_mov_b32_e32 v36, v65
	v_pk_mul_f32 v[4:5], v[8:9], v[4:5]
	v_pk_mul_f32 v[8:9], v[36:37], v[2:3] op_sel_hi:[1,0]
	v_cvt_pk_bf16_f32 v4, v4, v5
	v_pk_mul_f32 v[6:7], v[8:9], v[6:7]
	v_mov_b32_e32 v8, v66
	v_cvt_pk_bf16_f32 v5, v6, v7
	flat_store_dwordx2 v[128:129], v[4:5] offset:128
	global_load_dwordx4 v[230:233], v34, s[20:21] offset:288
	global_load_dwordx4 v[234:237], v34, s[20:21] offset:320
	global_load_dwordx4 v[238:241], v34, s[20:21] offset:352
	global_load_dwordx4 v[242:245], v34, s[20:21] offset:384
	global_load_dwordx4 v[246:249], v34, s[20:21] offset:416
	global_load_dwordx4 v[250:253], v34, s[20:21] offset:448
	global_load_dwordx4 v[216:219], v34, s[20:21] offset:480
	v_mov_b32_e32 v9, v38
	v_pk_mul_f32 v[8:9], v[8:9], v[2:3] op_sel_hi:[1,0]
	v_mov_b32_e32 v38, v67
	s_waitcnt vmcnt(0)
	v_mov_b64_e32 v[4:5], v[230:231]
	v_mov_b64_e32 v[6:7], v[232:233]
	v_pk_mul_f32 v[4:5], v[8:9], v[4:5]
	v_pk_mul_f32 v[8:9], v[38:39], v[2:3] op_sel_hi:[1,0]
	v_cvt_pk_bf16_f32 v4, v4, v5
	v_pk_mul_f32 v[6:7], v[8:9], v[6:7]
	v_mov_b32_e32 v8, v42
	v_cvt_pk_bf16_f32 v5, v6, v7
	flat_store_dwordx2 v[128:129], v[4:5] offset:144
	v_mov_b64_e32 v[4:5], v[234:235]
	v_mov_b64_e32 v[6:7], v[236:237]
	v_mov_b32_e32 v9, v40
	v_pk_mul_f32 v[8:9], v[8:9], v[2:3] op_sel_hi:[1,0]
	v_mov_b32_e32 v40, v43
	v_pk_mul_f32 v[4:5], v[8:9], v[4:5]
	v_pk_mul_f32 v[8:9], v[40:41], v[2:3] op_sel_hi:[1,0]
	v_cvt_pk_bf16_f32 v4, v4, v5
	v_pk_mul_f32 v[6:7], v[8:9], v[6:7]
	v_mov_b32_e32 v8, v46
	v_cvt_pk_bf16_f32 v5, v6, v7
	flat_store_dwordx2 v[128:129], v[4:5] offset:160
	v_mov_b64_e32 v[4:5], v[238:239]
	v_mov_b64_e32 v[6:7], v[240:241]
	v_mov_b32_e32 v9, v44
	v_pk_mul_f32 v[8:9], v[8:9], v[2:3] op_sel_hi:[1,0]
	v_mov_b32_e32 v44, v47
	v_pk_mul_f32 v[4:5], v[8:9], v[4:5]
	v_pk_mul_f32 v[8:9], v[44:45], v[2:3] op_sel_hi:[1,0]
	v_cvt_pk_bf16_f32 v4, v4, v5
	v_pk_mul_f32 v[6:7], v[8:9], v[6:7]
	v_mov_b32_e32 v8, v48
	v_cvt_pk_bf16_f32 v5, v6, v7
	flat_store_dwordx2 v[128:129], v[4:5] offset:176
	v_mov_b64_e32 v[4:5], v[242:243]
	v_mov_b64_e32 v[6:7], v[244:245]
	v_mov_b32_e32 v9, v20
	v_pk_mul_f32 v[8:9], v[8:9], v[2:3] op_sel_hi:[1,0]
	v_mov_b32_e32 v20, v49
	v_pk_mul_f32 v[4:5], v[8:9], v[4:5]
	v_pk_mul_f32 v[8:9], v[20:21], v[2:3] op_sel_hi:[1,0]
	v_cvt_pk_bf16_f32 v4, v4, v5
	v_pk_mul_f32 v[6:7], v[8:9], v[6:7]
	v_mov_b32_e32 v8, v50
	v_cvt_pk_bf16_f32 v5, v6, v7
	flat_store_dwordx2 v[128:129], v[4:5] offset:192
	v_mov_b64_e32 v[4:5], v[246:247]
	v_mov_b64_e32 v[6:7], v[248:249]
	v_mov_b32_e32 v9, v22
	v_pk_mul_f32 v[8:9], v[8:9], v[2:3] op_sel_hi:[1,0]
	v_mov_b32_e32 v22, v51
	v_pk_mul_f32 v[4:5], v[8:9], v[4:5]
	v_pk_mul_f32 v[8:9], v[22:23], v[2:3] op_sel_hi:[1,0]
	v_cvt_pk_bf16_f32 v4, v4, v5
	v_pk_mul_f32 v[6:7], v[8:9], v[6:7]
	v_mov_b32_e32 v8, v106
	v_cvt_pk_bf16_f32 v5, v6, v7
	flat_store_dwordx2 v[128:129], v[4:5] offset:208
	v_mov_b64_e32 v[4:5], v[250:251]
	v_mov_b64_e32 v[6:7], v[252:253]
	v_mov_b32_e32 v9, v26
	v_pk_mul_f32 v[8:9], v[8:9], v[2:3] op_sel_hi:[1,0]
	v_mov_b32_e32 v26, v107
	v_pk_mul_f32 v[4:5], v[8:9], v[4:5]
	v_pk_mul_f32 v[8:9], v[26:27], v[2:3] op_sel_hi:[1,0]
	v_cvt_pk_bf16_f32 v4, v4, v5
	v_pk_mul_f32 v[6:7], v[8:9], v[6:7]
	v_mov_b32_e32 v8, v30
	v_cvt_pk_bf16_f32 v5, v6, v7
	flat_store_dwordx2 v[128:129], v[4:5] offset:224
	v_mov_b64_e32 v[4:5], v[216:217]
	v_mov_b64_e32 v[6:7], v[218:219]
	v_mov_b32_e32 v9, v28
	v_pk_mul_f32 v[8:9], v[8:9], v[2:3] op_sel_hi:[1,0]
	v_mov_b32_e32 v28, v31
	v_pk_mul_f32 v[4:5], v[8:9], v[4:5]
	v_pk_mul_f32 v[8:9], v[28:29], v[2:3] op_sel_hi:[1,0]
	v_cvt_pk_bf16_f32 v4, v4, v5
	v_pk_mul_f32 v[6:7], v[8:9], v[6:7]
	s_nop 0
	v_cvt_pk_bf16_f32 v5, v6, v7
	flat_store_dwordx2 v[128:129], v[4:5] offset:240
